# MLA fast88 loop: K tiles prefetched one tile further (3 LDS slots kept), V issued before K, end-of-tile vmcnt(1) leaves the newest K piece in flight; on top of hoist + deferred PV MFMA
# baseline (speedup 1.0000x reference)
; #define ALAS __attribute__((address_space(3)))
; #define ATT_WAIT_BAR() asm volatile("s_waitcnt vmcnt(0) lgkmcnt(0)\n\ts_barrier" ::: "memory")
; #define MF_ISSUE_K(t, s) do { glds16(ksrc + (long)(t) * 64 * 512, (unsigned)__builtin_amdgcn_readfirstlane(kdst + (s) * KSLOT)); \
;         if (wid < 4) glds16(krsrc + (long)(t) * 64 * 32, (unsigned)__builtin_amdgcn_readfirstlane(krdst + (s) * KSLOT)); } while (0)
; __device__ __forceinline__ bool mla_unit_fast88(const Args& A, int b, int h, int qb, ALAS char* shm, const int tidb) {
;     ...
;     const int t_end = 4 * qb + 4;
;     const int cw = 4 * qb + (wid >> 1);
;     if (tid == 0) bailw[0] = 0;
;     MF_ISSUE_K(0, 0); MF_ISSUE_V(0, 0); MF_ISSUE_K(1, 1);
;     const unsigned char* Q8w = A.Q8 + (rowbase + q0 + wid * 32 + r32) * 768 + h * 96;
;     const unsigned char* Q8r = hi == 0 ? Q8w + 64 : A.ZERO;
;     v8i qf0, qf1;
;     { const u32x4 a0 = *(const u32x4*)(Q8w + 32 * hi), a1 = *(const u32x4*)(Q8w + 32 * hi + 16), b0 = *(const u32x4*)(Q8r), b1 = *(const u32x4*)(Q8r + 16);
;       qf0 = (v8i){(int)a0.x, (int)a0.y, (int)a0.z, (int)a0.w, (int)a1.x, (int)a1.y, (int)a1.z, (int)a1.w}; qf1 = (v8i){(int)b0.x, (int)b0.y, (int)b0.z, (int)b0.w, (int)b1.x, (int)b1.y, (int)b1.z, (int)b1.w}; }
;     const int sa8 = 0x7c7c7c7c, sb8 = 0x7b7b7b7b;
;     f32x16 o0 = {}, o1 = {}, ls = {};
;     const v8i ones8 = {0x38383838, 0x38383838, 0x38383838, 0x38383838, 0x38383838, 0x38383838, 0x38383838, 0x38383838};
;     const int vbo = ((lane >> 4) & 1) * 32 + (lane & 3) * 8 + (4 * hi + ((lane & 15) >> 2)) * 64;
;     ALAS const char* Kfr = shm + L_K + lane * 16;
;     ...
;     ATT_WAIT_BAR();
;     f32x16 cs[2][2];
;     { f32x16 z0 = {}, z1 = {}; ALAS const char* Ks_ = Kfr;
;       v8i k00, k01, k10, k11; M8_KFRAG(k00, Ks_, 0, 0); M8_KFRAG(k01, Ks_, 0, 1); M8_KFRAG(k10, Ks_, 1, 0); M8_KFRAG(k11, Ks_, 1, 1);
;       mfma8_acc(z0, k00, qf0, sa8, sb8); mfma8_acc(z1, k01, qf0, sa8, sb8); mfma8_acc(z0, k10, qf1, sa8, sb8); mfma8_acc(z1, k11, qf1, sa8, sb8);
;       asm volatile("s_nop 15\n\ts_nop 7" : "+v"(z0), "+v"(z1));
;       cs[0][0] = z0; cs[0][1] = z1; }
;     const float mhat = MF_ROWMAX(cs[0][0], cs[0][1]);
; #pragma unroll
;     for (int r = 0; r < 16; ++r) { cs[0][0][r] -= mhat; cs[0][1][r] -= mhat; }
;     f32x16 negm;
; #pragma unroll
;     for (int r = 0; r < 16; ++r) negm[r] = -mhat;
;     bool bailed = false; int ks = 0, vs = 0;
.LBB0_648:
	v_cmp_gt_u32_e32 vcc, 32, v154
	v_mov_b32_e32 v2, 0x800
	v_mov_b32_e32 v3, 0x8000
	v_cndmask_b32_e32 v2, 0, v2, vcc
	v_cndmask_b32_e64 v100, v2, v3, s[2:3]
	s_lshl_b32 s2, s6, 8
	v_mov_b32_e32 v101, v1
	s_lshl_b32 s37, s6, 2
	s_add_i32 s3, s45, 0x2000
	s_or_b32 s36, s30, s2
	s_lshl_b32 s2, s1, 5
	s_add_i32 s0, s37, 4
	s_add_i32 s47, s47, s37
	v_lshl_add_u64 v[2:3], v[146:147], 0, v[100:101]
	s_mov_b32 s4, m0
	s_mov_b32 m0, s3
	s_nop 0
	global_load_lds_dwordx4 v[2:3], off
	s_mov_b32 m0, s4
	s_add_i32 s3, s45, 0x4000
	v_lshl_add_u64 v[2:3], v[2:3], 0, v[100:101]
	s_mov_b32 s4, m0
	s_mov_b32 m0, s3
	s_nop 0
	global_load_lds_dwordx4 v[2:3], off
	s_mov_b32 m0, s4
	s_ashr_i32 s3, s2, 31
	s_add_u32 s24, s36, s2
	v_or_b32_e32 v4, s24, v156
	v_mov_b64_e32 v[2:3], s[74:75]
	s_addc_u32 s25, s31, s3
	v_mad_u64_u32 v[2:3], s[2:3], v4, s67, v[2:3]
	v_mov_b32_e32 v4, 0x300
	v_mad_i32_i24 v3, s25, v4, v3
	v_lshl_add_u64 v[4:5], v[2:3], 0, 64
	v_mov_b32_e32 v6, s27
	v_cndmask_b32_e32 v5, v6, v5, vcc
	v_mov_b32_e32 v6, s26
	v_lshl_add_u64 v[2:3], v[2:3], 0, v[0:1]
	v_cndmask_b32_e32 v4, v6, v4, vcc
	global_load_dwordx4 v[134:137], v[2:3], off offset:16
	global_load_dwordx4 v[130:133], v[2:3], off
	global_load_dwordx4 v[142:145], v[4:5], off offset:16
	global_load_dwordx4 v[138:141], v[4:5], off
	v_lshlrev_b32_e32 v155, 4, v154
	s_mov_b32 s4, 0
	v_add_u32_e32 v157, 0, v155
	s_waitcnt vmcnt(0) lgkmcnt(0)
	s_barrier
	s_mov_b32 s18, s4
	s_mov_b32 s19, s4
	ds_read_b128 v[50:53], v157
	ds_read_b128 v[54:57], v157 offset:1024
	ds_read_b128 v[58:61], v157 offset:2048
	ds_read_b128 v[62:65], v157 offset:3072
	ds_read_b128 v[66:69], v157 offset:4096
	ds_read_b128 v[70:73], v157 offset:5120
	ds_read_b128 v[74:77], v157 offset:6144
	ds_read_b128 v[78:81], v157 offset:7168
	s_mov_b32 s5, s4
	s_mov_b32 s6, s4
	s_mov_b32 s7, s4
	s_mov_b32 s8, s4
	s_mov_b32 s9, s4
	s_mov_b32 s10, s4
	s_mov_b32 s11, s4
	s_mov_b32 s12, s4
	s_mov_b32 s13, s4
	s_mov_b32 s14, s4
	s_mov_b32 s15, s4
	s_mov_b32 s16, s4
	s_mov_b32 s17, s4
	v_mov_b64_e32 v[32:33], s[18:19]
	v_mov_b64_e32 v[30:31], s[16:17]
	v_mov_b64_e32 v[28:29], s[14:15]
	v_mov_b64_e32 v[26:27], s[12:13]
	v_mov_b64_e32 v[24:25], s[10:11]
	v_mov_b64_e32 v[22:23], s[8:9]
	v_mov_b64_e32 v[20:21], s[6:7]
	v_mov_b64_e32 v[18:19], s[4:5]
	v_mov_b64_e32 v[48:49], v[32:33]
	v_mov_b64_e32 v[46:47], v[30:31]
	v_mov_b64_e32 v[44:45], v[28:29]
	v_mov_b64_e32 v[42:43], v[26:27]
	v_mov_b64_e32 v[40:41], v[24:25]
	v_mov_b64_e32 v[38:39], v[22:23]
	v_mov_b64_e32 v[36:37], v[20:21]
	v_mov_b64_e32 v[34:35], v[18:19]
	v_mov_b32_e32 v16, v1
	v_mov_b32_e32 v17, v1
	v_mov_b32_e32 v2, v1
	v_mov_b32_e32 v3, v1
	v_mov_b32_e32 v4, v1
	v_mov_b32_e32 v5, v1
	v_mov_b32_e32 v6, v1
	v_mov_b32_e32 v7, v1
	v_mov_b32_e32 v8, v1
	v_mov_b32_e32 v9, v1
	v_mov_b32_e32 v10, v1
	v_mov_b32_e32 v11, v1
	v_mov_b32_e32 v12, v1
	v_mov_b32_e32 v13, v1
	v_mov_b32_e32 v14, v1
	v_mov_b32_e32 v15, v1
	s_mov_b32 s41, s31
	s_mov_b32 s5, 3
	v_mul_hi_u32_u24_e32 v149, 3, v100
	v_mul_u32_u24_e32 v148, 3, v100
	v_lshl_add_u64 v[150:151], v[98:99], 0, s[78:79]
	s_waitcnt vmcnt(0) lgkmcnt(0)
	v_mfma_scale_f32_32x32x64_f8f6f4 v[34:49], v[50:57], v[130:137], v[34:49], v247, v253 op_sel_hi:[0,0,0]
	s_waitcnt lgkmcnt(4)
	v_mfma_scale_f32_32x32x64_f8f6f4 v[18:33], v[58:65], v[130:137], v[18:33], v247, v253 op_sel_hi:[0,0,0]
	s_waitcnt vmcnt(0) lgkmcnt(2)
	v_mfma_scale_f32_32x32x64_f8f6f4 v[34:49], v[66:73], v[138:145], v[34:49], v247, v253 op_sel_hi:[0,0,0]
	s_waitcnt lgkmcnt(0)
	v_mfma_scale_f32_32x32x64_f8f6f4 v[18:33], v[74:81], v[138:145], v[18:33], v247, v253 op_sel_hi:[0,0,0]
	s_nop 0
	s_nop 15
	s_nop 7
	s_nop 0
	v_max3_f32 v0, v34, v18, v38
	s_nop 0
	v_max3_f32 v0, v0, v22, v42
	s_nop 0
	v_max3_f32 v0, v0, v26, v46
	s_nop 0
	v_max_f32_e32 v0, v0, v30
	v_max3_f32 v50, v35, v19, v39
	s_nop 0
	v_max3_f32 v50, v50, v23, v43
	s_nop 0
	v_max3_f32 v50, v50, v27, v47
	s_nop 0
	v_max_f32_e32 v50, v50, v31
	v_max3_f32 v51, v36, v20, v40
	s_nop 0
	v_max3_f32 v51, v51, v24, v44
	s_nop 0
	v_max3_f32 v51, v51, v28, v48
	s_nop 0
	v_max_f32_e32 v51, v51, v32
	v_max3_f32 v52, v37, v21, v41
	s_nop 0
	v_max3_f32 v52, v52, v25, v45
	s_nop 0
	v_max3_f32 v52, v52, v29, v49
	s_nop 0
	v_max_f32_e32 v52, v52, v33
	v_max3_f32 v0, v0, v50, v51
	s_nop 0
	v_max_f32_e32 v0, v0, v52
	s_nop 0
	v_mov_b32_e32 v50, v0
	s_nop 1
	v_permlane32_swap_b32_e32 v0, v50
	v_max_f32_e32 v50, v50, v50
	v_max_f32_e32 v0, v0, v0
	v_max_f32_e32 v0, v0, v50
	v_sub_f32_e32 v65, v49, v0
	v_sub_f32_e32 v64, v48, v0
	v_sub_f32_e32 v63, v47, v0
	v_sub_f32_e32 v62, v46, v0
	v_sub_f32_e32 v61, v45, v0
	v_sub_f32_e32 v60, v44, v0
	v_sub_f32_e32 v59, v43, v0
	v_sub_f32_e32 v58, v42, v0
	v_sub_f32_e32 v57, v41, v0
	v_sub_f32_e32 v56, v40, v0
	v_sub_f32_e32 v55, v39, v0
	v_sub_f32_e32 v54, v38, v0
	v_sub_f32_e32 v53, v37, v0
	v_sub_f32_e32 v52, v36, v0
	v_sub_f32_e32 v51, v35, v0
	v_sub_f32_e32 v50, v34, v0
	v_sub_f32_e32 v97, v33, v0
	v_sub_f32_e32 v96, v32, v0
	v_sub_f32_e32 v95, v31, v0
	v_sub_f32_e32 v94, v30, v0
	v_sub_f32_e32 v93, v29, v0
	v_sub_f32_e32 v92, v28, v0
	v_sub_f32_e32 v91, v27, v0
	v_sub_f32_e32 v90, v26, v0
	v_sub_f32_e32 v89, v25, v0
	v_sub_f32_e32 v88, v24, v0
	v_sub_f32_e32 v87, v23, v0
	v_sub_f32_e32 v86, v22, v0
	v_sub_f32_e32 v85, v21, v0
	v_sub_f32_e32 v84, v20, v0
	v_sub_f32_e32 v83, v19, v0
	v_sub_f32_e32 v82, v18, v0
	v_xor_b32_e32 v66, 0x80000000, v0
	v_mov_b64_e32 v[32:33], v[16:17]
	v_mov_b64_e32 v[48:49], v[16:17]
	v_mov_b32_e32 v67, v66
	v_mov_b32_e32 v68, v66
	v_mov_b32_e32 v69, v66
	v_mov_b32_e32 v70, v66
	v_mov_b32_e32 v71, v66
	v_mov_b32_e32 v72, v66
	v_mov_b32_e32 v73, v66
	v_mov_b32_e32 v74, v66
	v_mov_b32_e32 v75, v66
	v_mov_b32_e32 v76, v66
	v_mov_b32_e32 v77, v66
	v_mov_b32_e32 v78, v66
	v_mov_b32_e32 v79, v66
	v_mov_b32_e32 v80, v66
	v_mov_b32_e32 v81, v66
	v_lshl_add_u64 v[146:147], v[146:147], 0, v[100:101]
	s_barrier
	v_lshlrev_b32_e32 v0, 1, v100
	v_mov_b64_e32 v[30:31], v[14:15]
	v_mov_b64_e32 v[28:29], v[12:13]
	v_mov_b64_e32 v[26:27], v[10:11]
	v_mov_b64_e32 v[24:25], v[8:9]
	v_mov_b64_e32 v[22:23], v[6:7]
	v_mov_b64_e32 v[20:21], v[4:5]
	v_mov_b64_e32 v[18:19], v[2:3]
	v_mov_b64_e32 v[46:47], v[14:15]
	v_mov_b64_e32 v[44:45], v[12:13]
	v_mov_b64_e32 v[42:43], v[10:11]
	v_mov_b64_e32 v[40:41], v[8:9]
	v_mov_b64_e32 v[38:39], v[6:7]
	v_mov_b64_e32 v[36:37], v[4:5]
	v_mov_b64_e32 v[34:35], v[2:3]
	v_mov_b32_e32 v172, 0
	v_mov_b32_e32 v173, 0
	v_mov_b32_e32 v174, 0
	v_mov_b32_e32 v175, 0
	v_mov_b32_e32 v176, 0
	v_mov_b32_e32 v177, 0
	v_mov_b32_e32 v178, 0
	v_mov_b32_e32 v179, 0
	v_mov_b32_e32 v180, 0
	v_mov_b32_e32 v181, 0
	v_mov_b32_e32 v182, 0
	v_mov_b32_e32 v183, 0
	v_mov_b32_e32 v184, 0
	v_mov_b32_e32 v185, 0
	v_mov_b32_e32 v186, 0
	v_mov_b32_e32 v187, 0
; #define ALAS __attribute__((address_space(3)))
; #define MF_ISSUE_K(t, s) do { glds16(ksrc + (long)(t) * 64 * 512, (unsigned)__builtin_amdgcn_readfirstlane(kdst + (s) * KSLOT)); \
;         if (wid < 4) glds16(krsrc + (long)(t) * 64 * 32, (unsigned)__builtin_amdgcn_readfirstlane(krdst + (s) * KSLOT)); } while (0)
; #define MF_ISSUE_V(t, s) glds16(vsrc + (long)(t) * 64 * 512, (unsigned)__builtin_amdgcn_readfirstlane(vdst + (s) * VSLOT))
; #define MF_ISSUE_K(t, s) glds16(ks8 + (long)(t) * kst8, (unsigned)__builtin_amdgcn_readfirstlane(kdst + (s) * KSLOT))
; #define MF_ISSUE_V(t, s) glds16(vsrc + (long)(t) * 64 * 512, (unsigned)__builtin_amdgcn_readfirstlane(vdst + (s) * VSLOT))
; #define M8_KFRAG(dst, base, m, kh) do { const u32x4 lo_ = *(ALAS const u32x4*)((base) + (((m) * 2 + (kh)) * 2) * 1024), hi_ = *(ALAS const u32x4*)((base) + (((m) * 2 + (kh)) * 2 + 1) * 1024); \
;         dst = (v8i){(int)lo_.x, (int)lo_.y, (int)lo_.z, (int)lo_.w, (int)hi_.x, (int)hi_.y, (int)hi_.z, (int)hi_.w}; } while (0)
; #define MF_ISSUE_K(t, s) glds16(ks8 + (long)(t) * kst8, (unsigned)__builtin_amdgcn_readfirstlane(kdst + (s) * KSLOT))
; #define MF_ISSUE_V(t, s) do { if (wid < 4) glds16(vs8 + (long)(t) * 4096, (unsigned)__builtin_amdgcn_readfirstlane(vdst + (s) * 4096)); } while (0)
; #define M8_KFRAG(dst, base, m, kh) do { const u32x4 lo_ = *(ALAS const u32x4*)((base) + (((m) * 2 + (kh)) * 2) * 1024), hi_ = *(ALAS const u32x4*)((base) + (((m) * 2 + (kh)) * 2 + 1) * 1024); \
;         dst = (v8i){(int)lo_.x, (int)lo_.y, (int)lo_.z, (int)lo_.w, (int)hi_.x, (int)hi_.y, (int)hi_.z, (int)hi_.w}; } while (0)
; __device__ __forceinline__ bool mla_unit_fast88(const Args& A, int b, int h, int qb, ALAS char* shm, const int tidb) {
;     ...
;         for (int p = 0; p < 2; ++p) {
;             const int t = t2 + p; f32x16 &C0 = cs[p][0], &C1 = cs[p][1], &N0 = cs[p ^ 1][0], &N1 = cs[p ^ 1][1];
;             const bool vis = !bailed && t <= cw;
;             const int ks1 = ks == 2 ? 0 : ks + 1, ks2 = ks1 == 2 ? 0 : ks1 + 1;
;             if (t + 2 < t_end) MF_ISSUE_K(t + 2, ks2);
;             if (t + 1 < t_end) MF_ISSUE_V(t + 1, vs ^ 1);
;             if (vis) {
;                 {
;                     ALAS const char* Ks_ = Kfr + ks1 * KSLOT;
;                     v8i kfa, kfb; M8_KFRAG(kfa, Ks_, 0, 0);
;                     M8_KFRAG(kfb, Ks_, 0, 1);
.LBB0_649:
	s_add_i32 s2, s4, 1
	s_cmp_lg_u32 s4, 2
	s_cselect_b32 s4, s2, 0
	v_lshl_add_u32 v171, s4, 13, v157
	ds_read_b128 v[114:117], v171
	ds_read_b128 v[118:121], v171 offset:1024
	ds_read_b128 v[164:167], v171 offset:2048
	ds_read_b128 v[168:171], v171 offset:3072
	v_mfma_scale_f32_32x32x64_f8f6f4 v[18:33], v[180:187], v[172:179], v[18:33], v251, v247 op_sel_hi:[0,0,0] cbsz:1
	s_add_i32 s6, s5, -1
	s_cmp_lt_u32 s6, s0
	s_cselect_b64 s[2:3], -1, 0
	v_lshl_add_u64 v[152:153], v[146:147], 0, v[0:1]
	s_add_i32 s7, s5, -2
	s_cmp_ge_u32 s7, s0
	s_cselect_b64 s[8:9], -1, 0
	s_xor_b64 s[10:11], s[34:35], -1
	s_or_b64 s[8:9], s[10:11], s[8:9]
	s_and_b64 vcc, exec, s[8:9]
	s_cbranch_vccnz .Lmla_k0
	s_add_i32 s7, s45, 0xa000
	s_mov_b32 s8, m0
	s_mov_b32 m0, s7
	s_nop 0
	global_load_lds_dwordx4 v[150:151], off
	s_mov_b32 m0, s8
.Lmla_k0:
	s_cmp_lt_u32 s5, s0
	s_cbranch_scc0 .LBB0_653
	s_add_i32 s7, s4, 2
	s_add_i32 s8, s4, -1
	s_cmp_lt_u32 s7, 3
	s_cselect_b32 s7, s7, s8
	s_lshl_b32 s7, s7, 13
	v_lshl_add_u64 v[158:159], v[146:147], 0, v[0:1]
	s_add_i32 s7, s7, s45
	s_mov_b32 s8, m0
	s_mov_b32 m0, s7
	s_nop 0
	global_load_lds_dwordx4 v[158:159], off
	s_mov_b32 m0, s8

; #define ALAS __attribute__((address_space(3)))
; #define ATT_WAIT_BAR() asm volatile("s_waitcnt vmcnt(0) lgkmcnt(0)\n\ts_barrier" ::: "memory")
; #define MF_ISSUE_K(t, s) do { glds16(ksrc + (long)(t) * 64 * 512, (unsigned)__builtin_amdgcn_readfirstlane(kdst + (s) * KSLOT)); \
;         if (wid < 4) glds16(krsrc + (long)(t) * 64 * 32, (unsigned)__builtin_amdgcn_readfirstlane(krdst + (s) * KSLOT)); } while (0)
; #define MF_ISSUE_V(t, s) glds16(vsrc + (long)(t) * 64 * 512, (unsigned)__builtin_amdgcn_readfirstlane(vdst + (s) * VSLOT))
; #define MF_ISSUE_K(t, s) glds16(ks8 + (long)(t) * kst8, (unsigned)__builtin_amdgcn_readfirstlane(kdst + (s) * KSLOT))
; #define MF_ISSUE_V(t, s) glds16(vsrc + (long)(t) * 64 * 512, (unsigned)__builtin_amdgcn_readfirstlane(vdst + (s) * VSLOT))
; #define M8_KFRAG(dst, base, m, kh) do { const u32x4 lo_ = *(ALAS const u32x4*)((base) + (((m) * 2 + (kh)) * 2) * 1024), hi_ = *(ALAS const u32x4*)((base) + (((m) * 2 + (kh)) * 2 + 1) * 1024); \
;         dst = (v8i){(int)lo_.x, (int)lo_.y, (int)lo_.z, (int)lo_.w, (int)hi_.x, (int)hi_.y, (int)hi_.z, (int)hi_.w}; } while (0)
; #define MF_ISSUE_K(t, s) glds16(ks8 + (long)(t) * kst8, (unsigned)__builtin_amdgcn_readfirstlane(kdst + (s) * KSLOT))
; #define MF_ISSUE_V(t, s) do { if (wid < 4) glds16(vs8 + (long)(t) * 4096, (unsigned)__builtin_amdgcn_readfirstlane(vdst + (s) * 4096)); } while (0)
; __device__ __forceinline__ bool mla_unit_fast88(const Args& A, int b, int h, int qb, ALAS char* shm, const int tidb) {
;     ...
;         for (int p = 0; p < 2; ++p) {
;             const int t = t2 + p; f32x16 &C0 = cs[p][0], &C1 = cs[p][1], &N0 = cs[p ^ 1][0], &N1 = cs[p ^ 1][1];
;             const bool vis = !bailed && t <= cw;
;             const int ks1 = ks == 2 ? 0 : ks + 1, ks2 = ks1 == 2 ? 0 : ks1 + 1;
;             if (t + 2 < t_end) MF_ISSUE_K(t + 2, ks2);
;             if (t + 1 < t_end) MF_ISSUE_V(t + 1, vs ^ 1);
;             if (vis) {
;                 {
;                     ALAS const char* Ks_ = Kfr + ks1 * KSLOT;
;                     v8i kfa, kfb; M8_KFRAG(kfa, Ks_, 0, 0);
;                     M8_KFRAG(kfb, Ks_, 0, 1);
;     ...
;             ATT_WAIT_BAR();
.LBB0_655:
	s_add_i32 s8, s4, 1
	s_cmp_lt_u32 s5, s0
	s_cbranch_scc1 .Lmla_w0a
	s_waitcnt vmcnt(0)
	s_branch .Lmla_w0b
.Lmla_w0a:
	s_waitcnt vmcnt(1)
.Lmla_w0b:
	s_waitcnt lgkmcnt(0)
	s_barrier
	s_cmp_lg_u32 s4, 2
	s_cselect_b32 s4, s8, 0
	v_lshl_add_u32 v171, s4, 13, v157
	ds_read_b128 v[82:85], v171
	ds_read_b128 v[86:89], v171 offset:1024
	ds_read_b128 v[164:167], v171 offset:2048
	ds_read_b128 v[168:171], v171 offset:3072
	v_mfma_scale_f32_32x32x64_f8f6f4 v[18:33], v[180:187], v[172:179], v[18:33], v251, v247 op_sel_hi:[0,0,0] cbsz:1
	s_and_b64 s[2:3], s[34:35], s[2:3]
	s_andn2_b64 vcc, exec, s[2:3]
	s_cbranch_vccnz .Lmla_k1
	v_lshl_add_u64 v[158:159], v[150:151], 0, s[78:79]
	s_mov_b32 s2, m0
	s_mov_b32 m0, s46
	s_nop 0
	global_load_lds_dwordx4 v[158:159], off
	s_mov_b32 m0, s2
.Lmla_k1:
	s_add_i32 s8, s5, 1
	s_cmp_lt_u32 s8, s0
	s_cbranch_scc0 .LBB0_657
	s_add_i32 s8, s4, 2
	s_add_i32 s9, s4, -1
	s_cmp_lt_u32 s8, 3
	s_cselect_b32 s8, s8, s9
	s_lshl_b32 s8, s8, 13
	v_lshl_add_u64 v[146:147], v[146:147], 0, v[148:149]
	s_add_i32 s8, s8, s45
	s_mov_b32 s9, m0
	s_mov_b32 m0, s8
	s_nop 0
	global_load_lds_dwordx4 v[146:147], off
	s_mov_b32 m0, s9

; #define ATT_WAIT_BAR() asm volatile("s_waitcnt vmcnt(0) lgkmcnt(0)\n\ts_barrier" ::: "memory")
; __device__ __forceinline__ bool mla_unit_fast88(const Args& A, int b, int h, int qb, ALAS char* shm, const int tidb) {
;     ...
;             ATT_WAIT_BAR();
.LBB0_659:
	s_add_i32 s8, s5, 1
	s_cmp_lt_u32 s8, s0
	s_cbranch_scc1 .Lmla_w1a
	s_waitcnt vmcnt(0)
	s_branch .Lmla_w1b

; #define ATT_WAIT_BAR() asm volatile("s_waitcnt vmcnt(0) lgkmcnt(0)\n\ts_barrier" ::: "memory")
; __device__ __forceinline__ bool mla_unit_fast88(const Args& A, int b, int h, int qb, ALAS char* shm, const int tidb) {
;     ...
;             ks = ks1; vs ^= 1;
;             ATT_WAIT_BAR();
;         }
;     }
.Lmla_w1b:
	s_waitcnt lgkmcnt(0)
	s_barrier
	s_add_i32 s5, s5, 2
	s_cmp_ge_u32 s6, s0
	v_lshl_add_u64 v[150:151], v[150:151], 0, s[80:81]
	s_cbranch_scc1 .LBB0_665
	v_mov_b64_e32 v[146:147], v[152:153]
	s_branch .LBB0_649

; #define MF_ISSUE_K(t, s) do { glds16(ksrc + (long)(t) * 64 * 512, (unsigned)__builtin_amdgcn_readfirstlane(kdst + (s) * KSLOT)); \
;         if (wid < 4) glds16(krsrc + (long)(t) * 64 * 32, (unsigned)__builtin_amdgcn_readfirstlane(krdst + (s) * KSLOT)); } while (0)
; #define MF_ISSUE_V(t, s) glds16(vsrc + (long)(t) * 64 * 512, (unsigned)__builtin_amdgcn_readfirstlane(vdst + (s) * VSLOT))
; #define MF_ISSUE_K(t, s) glds16(ks8 + (long)(t) * kst8, (unsigned)__builtin_amdgcn_readfirstlane(kdst + (s) * KSLOT))
; #define MF_ISSUE_V(t, s) glds16(vsrc + (long)(t) * 64 * 512, (unsigned)__builtin_amdgcn_readfirstlane(vdst + (s) * VSLOT))
; #define MF_ISSUE_K(t, s) glds16(ks8 + (long)(t) * kst8, (unsigned)__builtin_amdgcn_readfirstlane(kdst + (s) * KSLOT))
; #define MF_ISSUE_V(t, s) do { if (wid < 4) glds16(vs8 + (long)(t) * 4096, (unsigned)__builtin_amdgcn_readfirstlane(vdst + (s) * 4096)); } while (0)
; __device__ __forceinline__ bool mla_unit_fast88(const Args& A, int b, int h, int qb, ALAS char* shm, const int tidb) {
;     ...
;             const bool vis = !bailed && t <= cw;
;             const int ks1 = ks == 2 ? 0 : ks + 1, ks2 = ks1 == 2 ? 0 : ks1 + 1;
;             if (t + 2 < t_end) MF_ISSUE_K(t + 2, ks2);
;             if (t + 1 < t_end) MF_ISSUE_V(t + 1, vs ^ 1);
;             if (vis) {
.Lmla_nv1:
	v_mov_b32_e32 v180, 0
	v_mov_b32_e32 v181, 0
	v_mov_b32_e32 v182, 0
	v_mov_b32_e32 v183, 0
	v_mov_b32_e32 v184, 0
	v_mov_b32_e32 v185, 0
	v_mov_b32_e32 v186, 0
	v_mov_b32_e32 v187, 0
	s_branch .LBB0_659
.LBB0_663:
	s_andn2_b64 vcc, exec, s[4:5]
	v_and_b32_e32 v0, 32, v7
	s_cbranch_vccnz .LBB0_644
